# v58 + static s_setprio 1 for waves 4-7 during the P4 selection loops (reset to 0 after each pass)
# baseline (speedup 1.0000x reference)
; #define LAS __attribute__((address_space(3)))
; __device__ __forceinline__ bf16 f2bf(float f) { unsigned u = __float_as_uint(f); return (bf16)((u + 0x7fffu + ((u >> 16) & 1u)) >> 16); }
; #define DSA2_LOADK(dst, kt_) do { _Pragma("unroll") for (int s = 0; s < 4; ++s) dst[s] = *(const bf16x8*)(kp + (size_t)(32 * (kt_)) * Y0P + 16 * s); } while (0)
; template <int STAGE>
; __device__ __forceinline__ void pass2(LAS unsigned char* lds, const bf16* kbase, int g, int t0, const bf16x8 (&qf)[4][4], const f32x4 lo4, const f32x4 hi4, int wave, int r, int h2) {
;     ...
;     int kt = wave;
;     if (kt <= g) DSA2_LOADK(kf, kt);
; __device__ __forceinline__ bool run_unit2(LAS unsigned char* lds, const bf16* y0, const float* aux, unsigned* maskg, int b, int g, int tid_in, int wave, int lane) {
;     ...
;     for (int i = tid; i < (OFF2_TB) / 4; i += NTHR) ((LAS unsigned*)lds)[i] = 0u;
;     if (tid < 32) { ((LAS unsigned*)(lds + OFF2_CNT))[tid] = 0u; }
;     if (tid == 0) ((LAS int*)(lds + OFF2_FLAG))[0] = 0;
;     bf16x8 qf[4][4];
;     {
;         const bf16* qp = y0 + (rowbase + t0 + r) * (size_t)Y0P + Y0_IQ + 8 * h2;
; #pragma unroll
;         for (int hd = 0; hd < 4; ++hd)
; #pragma unroll
;             for (int s = 0; s < 4; ++s) qf[hd][s] = *(const bf16x8*)(qp + hd * 64 + 16 * s);
;     }
;     const f32x4 w4 = *(const f32x4*)(aux + (rowbase + t0 + r) * 16 + 8);
;     f32x4 lo4, hi4;
; #pragma unroll
;     for (int hd = 0; hd < 4; ++hd) {
;         const float wsc = w4[hd] * 0.0625f;
;         lo4[hd] = (w4[hd] >= 0.f) ? 0.f : -INFINITY; hi4[hd] = (w4[hd] >= 0.f) ? INFINITY : 0.f;
; #pragma unroll
;         for (int s = 0; s < 4; ++s) {
;             bf16x8 a = qf[hd][s];
; #pragma unroll
;             for (int j = 0; j < 8; ++j) a[j] = (short)f2bf(__uint_as_float(((unsigned)(unsigned short)a[j]) << 16) * wsc);
;             qf[hd][s] = a;
;         }
;     }
;     const bf16* kbase = y0 + rowbase * (size_t)Y0P + Y0_IK;
;     __syncthreads();
.LBB0_779:
	s_or_b64 exec, exec, s[2:3]
	v_cmp_gt_i32_e32 vcc, 32, v206
	s_and_saveexec_b64 s[2:3], vcc
	v_lshl_add_u32 v0, v206, 2, 0
	v_add_u32_e32 v0, 0x18200, v0
	ds_write_b32 v0, v177
	s_or_b64 exec, exec, s[2:3]
	v_cmp_eq_u32_e32 vcc, 0, v206
	s_and_saveexec_b64 s[2:3], vcc
	v_mov_b32_e32 v0, s88
	ds_write_b32 v0, v177
	s_or_b64 exec, exec, s[2:3]
	s_andn2_b32 s64, 0xff, s0
	s_lshr_b32 s66, s0, 8
	v_and_b32_e32 v218, 31, v217
	s_lshl_b32 s41, s64, 5
	v_ashrrev_i32_e32 v219, 5, v217
	s_lshl_b64 s[76:77], s[66:67], 13
	v_or_b32_e32 v211, s41, v218
	v_or_b32_e32 v0, s76, v211
	v_mov_b64_e32 v[2:3], s[44:45]
	s_waitcnt vmcnt(0)
	v_lshlrev_b32_e32 v48, 3, v219
	v_mov_b32_e32 v1, s77
	v_mad_u64_u32 v[2:3], s[0:1], v0, s33, v[2:3]
	v_ashrrev_i32_e32 v49, 31, v48
	v_mad_u32_u24 v3, s77, v187, v3
	v_lshlrev_b64 v[50:51], 1, v[48:49]
	v_lshlrev_b64 v[0:1], 6, v[0:1]
	v_lshl_add_u64 v[2:3], v[2:3], 0, v[50:51]
	v_lshl_add_u64 v[0:1], s[46:47], 0, v[0:1]
	global_load_dwordx4 v[16:19], v[0:1], off offset:32
	v_add_co_u32_e32 v0, vcc, s31, v2
	s_mul_i32 s78, s66, 0x3800000
	s_nop 0
	v_addc_co_u32_e32 v1, vcc, 0, v3, vcc
	global_load_dwordx4 v[52:55], v[0:1], off offset:2048
	v_lshl_add_u64 v[0:1], v[2:3], 0, s[28:29]
	global_load_dwordx4 v[56:59], v[0:1], off offset:32
	global_load_dwordx4 v[60:63], v[0:1], off offset:64
	global_load_dwordx4 v[76:79], v[0:1], off offset:96
	global_load_dwordx4 v[80:83], v[0:1], off offset:128
	global_load_dwordx4 v[44:47], v[0:1], off offset:160
	global_load_dwordx4 v[40:43], v[0:1], off offset:192
	global_load_dwordx4 v[36:39], v[0:1], off offset:224
	global_load_dwordx4 v[32:35], v[0:1], off offset:256
	global_load_dwordx4 v[28:31], v[0:1], off offset:288
	global_load_dwordx4 v[24:27], v[0:1], off offset:320
	global_load_dwordx4 v[20:23], v[0:1], off offset:352
	global_load_dwordx4 v[12:15], v[0:1], off offset:384
	global_load_dwordx4 v[8:11], v[0:1], off offset:416
	global_load_dwordx4 v[4:7], v[0:1], off offset:448
	s_nop 0
	global_load_dwordx4 v[0:3], v[0:1], off offset:480
	s_mul_hi_u32 s79, s66, 0x3800000
	s_add_u32 s0, s44, s78
	s_addc_u32 s1, s45, s79
	s_add_u32 s80, s0, 0x1a00
	s_addc_u32 s81, s1, 0
	v_mul_u32_u24_e32 v176, 0x1c00, v218
	v_readlane_b32 s0, v254, 24
	s_cmp_le_u32 s0, s64
	s_cselect_b64 s[82:83], -1, 0
	s_cmp_gt_u32 s0, s64
	v_lshl_add_u64 v[180:181], s[80:81], 0, v[176:177]
	v_lshl_add_u64 v[180:181], v[180:181], 0, v[50:51]
	v_lshl_add_u64 v[180:181], v[180:181], 0, s[36:37]
	global_load_dwordx4 v[140:143], v[180:181], off
	global_load_dwordx4 v[136:139], v[180:181], off offset:32
	global_load_dwordx4 v[132:135], v[180:181], off offset:64
	global_load_dwordx4 v[128:131], v[180:181], off offset:96
	s_waitcnt lgkmcnt(0)
	s_barrier
	s_waitcnt vmcnt(4)
	v_and_b32_e32 v71, 0xffff0000, v57
	v_lshlrev_b32_e32 v70, 16, v57
	v_and_b32_e32 v57, 0xffff0000, v58
	v_and_b32_e32 v73, 0xffff0000, v59
	v_lshlrev_b32_e32 v72, 16, v59
	v_mul_f32_e32 v84, 0x3d800000, v16
	v_cmp_le_f32_e32 vcc, 0, v16
	v_and_b32_e32 v65, 0xffff0000, v52
	v_lshlrev_b32_e32 v64, 16, v52
	v_and_b32_e32 v67, 0xffff0000, v53
	v_lshlrev_b32_e32 v66, 16, v53
	v_and_b32_e32 v53, 0xffff0000, v54
	v_lshlrev_b32_e32 v52, 16, v54
	v_and_b32_e32 v69, 0xffff0000, v55
	v_lshlrev_b32_e32 v68, 16, v55
	v_and_b32_e32 v55, 0xffff0000, v56
	v_lshlrev_b32_e32 v54, 16, v56
	v_lshlrev_b32_e32 v56, 16, v58
	v_pk_mul_f32 v[58:59], v[84:85], v[64:65] op_sel_hi:[0,1]
	v_pk_mul_f32 v[64:65], v[84:85], v[66:67] op_sel_hi:[0,1]
	v_pk_mul_f32 v[52:53], v[84:85], v[52:53] op_sel_hi:[0,1]
	v_pk_mul_f32 v[66:67], v[84:85], v[68:69] op_sel_hi:[0,1]
	v_pk_mul_f32 v[54:55], v[84:85], v[54:55] op_sel_hi:[0,1]
	v_pk_mul_f32 v[68:69], v[84:85], v[70:71] op_sel_hi:[0,1]
	v_pk_mul_f32 v[56:57], v[84:85], v[56:57] op_sel_hi:[0,1]
	v_pk_mul_f32 v[70:71], v[84:85], v[72:73] op_sel_hi:[0,1]
	v_bfe_u32 v16, v67, 16, 1
	v_bfe_u32 v72, v66, 16, 1
	v_bfe_u32 v73, v53, 16, 1
	v_bfe_u32 v74, v52, 16, 1
	v_bfe_u32 v75, v65, 16, 1
	v_bfe_u32 v85, v64, 16, 1
	v_bfe_u32 v86, v59, 16, 1
	v_bfe_u32 v87, v58, 16, 1
	v_add3_u32 v58, v58, v87, s73
	v_add3_u32 v59, v59, v86, s73
	v_add3_u32 v64, v64, v85, s73
	v_add3_u32 v65, v65, v75, s73
	v_add3_u32 v52, v52, v74, s73
	v_add3_u32 v53, v53, v73, s73
	v_add3_u32 v66, v66, v72, s73
	v_add3_u32 v16, v67, v16, s73
	v_bfe_u32 v88, v71, 16, 1
	v_bfe_u32 v89, v70, 16, 1
	v_bfe_u32 v90, v57, 16, 1
	v_bfe_u32 v91, v56, 16, 1
	v_perm_b32 v67, v16, v66, s72
	v_perm_b32 v66, v53, v52, s72
	v_perm_b32 v65, v65, v64, s72
	v_perm_b32 v64, v59, v58, s72
	v_bfe_u32 v16, v69, 16, 1
	v_bfe_u32 v52, v68, 16, 1
	v_bfe_u32 v53, v55, 16, 1
	v_bfe_u32 v58, v54, 16, 1
	v_add3_u32 v54, v54, v58, s73
	v_add3_u32 v53, v55, v53, s73
	v_add3_u32 v52, v68, v52, s73
	v_add3_u32 v16, v69, v16, s73
	v_add3_u32 v55, v56, v91, s73
	v_add3_u32 v56, v57, v90, s73
	v_add3_u32 v57, v70, v89, s73
	v_add3_u32 v58, v71, v88, s73
	v_perm_b32 v71, v58, v57, s72
	v_perm_b32 v70, v56, v55, s72
	v_perm_b32 v69, v16, v52, s72
	v_perm_b32 v68, v53, v54, s72
	v_and_b32_e32 v53, 0xffff0000, v60
	v_lshlrev_b32_e32 v52, 16, v60
	v_and_b32_e32 v55, 0xffff0000, v61
	v_lshlrev_b32_e32 v54, 16, v61
	v_and_b32_e32 v57, 0xffff0000, v62
	v_lshlrev_b32_e32 v56, 16, v62
	v_and_b32_e32 v59, 0xffff0000, v63
	v_lshlrev_b32_e32 v58, 16, v63
	v_pk_mul_f32 v[52:53], v[84:85], v[52:53] op_sel_hi:[0,1]
	v_pk_mul_f32 v[54:55], v[84:85], v[54:55] op_sel_hi:[0,1]
	v_pk_mul_f32 v[56:57], v[84:85], v[56:57] op_sel_hi:[0,1]
	v_pk_mul_f32 v[58:59], v[84:85], v[58:59] op_sel_hi:[0,1]
	v_bfe_u32 v16, v59, 16, 1
	v_bfe_u32 v60, v58, 16, 1
	v_bfe_u32 v61, v57, 16, 1
	v_bfe_u32 v62, v56, 16, 1
	v_bfe_u32 v63, v55, 16, 1
; __device__ __forceinline__ bf16 f2bf(float f) { unsigned u = __float_as_uint(f); return (bf16)((u + 0x7fffu + ((u >> 16) & 1u)) >> 16); }
; __device__ __forceinline__ bool run_unit2(LAS unsigned char* lds, const bf16* y0, const float* aux, unsigned* maskg, int b, int g, int tid_in, int wave, int lane) {
;     ...
;     const f32x4 w4 = *(const f32x4*)(aux + (rowbase + t0 + r) * 16 + 8);
;     f32x4 lo4, hi4;
; #pragma unroll
;     for (int hd = 0; hd < 4; ++hd) {
;         const float wsc = w4[hd] * 0.0625f;
;         lo4[hd] = (w4[hd] >= 0.f) ? 0.f : -INFINITY; hi4[hd] = (w4[hd] >= 0.f) ? INFINITY : 0.f;
; #pragma unroll
;         for (int s = 0; s < 4; ++s) {
;             bf16x8 a = qf[hd][s];
; #pragma unroll
;             for (int j = 0; j < 8; ++j) a[j] = (short)f2bf(__uint_as_float(((unsigned)(unsigned short)a[j]) << 16) * wsc);
;             qf[hd][s] = a;
;         }
;     }
	v_bfe_u32 v72, v54, 16, 1
	v_bfe_u32 v73, v53, 16, 1
	v_bfe_u32 v74, v52, 16, 1
	v_add3_u32 v52, v52, v74, s73
	v_add3_u32 v53, v53, v73, s73
	v_add3_u32 v54, v54, v72, s73
	v_add3_u32 v55, v55, v63, s73
	v_add3_u32 v56, v56, v62, s73
	v_add3_u32 v57, v57, v61, s73
	v_add3_u32 v58, v58, v60, s73
	v_add3_u32 v16, v59, v16, s73
	v_perm_b32 v75, v16, v58, s72
	v_perm_b32 v74, v57, v56, s72
	v_perm_b32 v73, v55, v54, s72
	v_perm_b32 v72, v53, v52, s72
	v_and_b32_e32 v53, 0xffff0000, v76
	v_lshlrev_b32_e32 v52, 16, v76
	v_and_b32_e32 v55, 0xffff0000, v77
	v_lshlrev_b32_e32 v54, 16, v77
	v_and_b32_e32 v57, 0xffff0000, v78
	v_lshlrev_b32_e32 v56, 16, v78
	v_and_b32_e32 v59, 0xffff0000, v79
	v_lshlrev_b32_e32 v58, 16, v79
	v_pk_mul_f32 v[52:53], v[84:85], v[52:53] op_sel_hi:[0,1]
	v_pk_mul_f32 v[54:55], v[84:85], v[54:55] op_sel_hi:[0,1]
	v_pk_mul_f32 v[56:57], v[84:85], v[56:57] op_sel_hi:[0,1]
	v_pk_mul_f32 v[58:59], v[84:85], v[58:59] op_sel_hi:[0,1]
	v_bfe_u32 v16, v59, 16, 1
	v_bfe_u32 v60, v58, 16, 1
	v_bfe_u32 v61, v57, 16, 1
	v_bfe_u32 v62, v56, 16, 1
	v_bfe_u32 v63, v55, 16, 1
	v_bfe_u32 v76, v54, 16, 1
	v_bfe_u32 v77, v53, 16, 1
	v_bfe_u32 v78, v52, 16, 1
	v_add3_u32 v52, v52, v78, s73
	v_add3_u32 v53, v53, v77, s73
	v_add3_u32 v54, v54, v76, s73
	v_add3_u32 v55, v55, v63, s73
	v_add3_u32 v56, v56, v62, s73
	v_add3_u32 v57, v57, v61, s73
	v_add3_u32 v58, v58, v60, s73
	v_add3_u32 v16, v59, v16, s73
	v_perm_b32 v79, v16, v58, s72
	v_perm_b32 v78, v57, v56, s72
	v_perm_b32 v77, v55, v54, s72
	v_perm_b32 v76, v53, v52, s72
	v_mul_f32_e32 v16, 0x3d800000, v17
	v_and_b32_e32 v53, 0xffff0000, v80
	v_lshlrev_b32_e32 v52, 16, v80
	v_and_b32_e32 v55, 0xffff0000, v81
	v_lshlrev_b32_e32 v54, 16, v81
	v_and_b32_e32 v57, 0xffff0000, v82
	v_lshlrev_b32_e32 v56, 16, v82
	v_pk_mul_f32 v[52:53], v[16:17], v[52:53] op_sel_hi:[0,1]
	v_pk_mul_f32 v[54:55], v[16:17], v[54:55] op_sel_hi:[0,1]
	v_pk_mul_f32 v[56:57], v[16:17], v[56:57] op_sel_hi:[0,1]
	v_and_b32_e32 v59, 0xffff0000, v83
	v_lshlrev_b32_e32 v58, 16, v83
	v_pk_mul_f32 v[58:59], v[16:17], v[58:59] op_sel_hi:[0,1]
	v_bfe_u32 v61, v57, 16, 1
	v_bfe_u32 v62, v56, 16, 1
	v_bfe_u32 v63, v55, 16, 1
	v_bfe_u32 v80, v54, 16, 1
	v_bfe_u32 v81, v53, 16, 1
	v_bfe_u32 v82, v52, 16, 1
	v_cndmask_b32_e64 v207, v188, 0, vcc
	v_cndmask_b32_e32 v208, 0, v189, vcc
	v_cmp_le_f32_e32 vcc, 0, v17
	v_bfe_u32 v17, v59, 16, 1
	v_add3_u32 v52, v52, v82, s73
	v_add3_u32 v53, v53, v81, s73
	v_add3_u32 v54, v54, v80, s73
	v_add3_u32 v55, v55, v63, s73
	v_add3_u32 v56, v56, v62, s73
	v_add3_u32 v57, v57, v61, s73
	v_bfe_u32 v60, v58, 16, 1
	v_add3_u32 v17, v59, v17, s73
	v_perm_b32 v82, v57, v56, s72
	v_perm_b32 v81, v55, v54, s72
	v_perm_b32 v80, v53, v52, s72
	v_and_b32_e32 v53, 0xffff0000, v44
	v_lshlrev_b32_e32 v52, 16, v44
	v_and_b32_e32 v55, 0xffff0000, v45
	v_lshlrev_b32_e32 v54, 16, v45
	v_and_b32_e32 v57, 0xffff0000, v47
	v_lshlrev_b32_e32 v56, 16, v47
	v_add3_u32 v58, v58, v60, s73
	v_pk_mul_f32 v[52:53], v[16:17], v[52:53] op_sel_hi:[0,1]
	v_pk_mul_f32 v[44:45], v[16:17], v[54:55] op_sel_hi:[0,1]
	v_and_b32_e32 v55, 0xffff0000, v46
	v_lshlrev_b32_e32 v54, 16, v46
	v_pk_mul_f32 v[46:47], v[16:17], v[56:57] op_sel_hi:[0,1]
	v_perm_b32 v83, v17, v58, s72
	v_pk_mul_f32 v[54:55], v[16:17], v[54:55] op_sel_hi:[0,1]
	v_bfe_u32 v17, v47, 16, 1
	v_bfe_u32 v56, v46, 16, 1
	v_bfe_u32 v61, v53, 16, 1
	v_bfe_u32 v62, v52, 16, 1
	v_bfe_u32 v59, v45, 16, 1
	v_bfe_u32 v60, v44, 16, 1
	v_add3_u32 v52, v52, v62, s73
	v_add3_u32 v53, v53, v61, s73
	v_add3_u32 v46, v46, v56, s73
	v_add3_u32 v17, v47, v17, s73
	v_add3_u32 v44, v44, v60, s73
	v_add3_u32 v45, v45, v59, s73
	v_perm_b32 v87, v17, v46, s72
	v_perm_b32 v84, v53, v52, s72
	v_and_b32_e32 v47, 0xffff0000, v41
	v_lshlrev_b32_e32 v46, 16, v41
	v_and_b32_e32 v53, 0xffff0000, v43
	v_lshlrev_b32_e32 v52, 16, v43
	v_bfe_u32 v57, v55, 16, 1
	v_bfe_u32 v58, v54, 16, 1
	v_perm_b32 v85, v45, v44, s72
	v_and_b32_e32 v45, 0xffff0000, v40
	v_lshlrev_b32_e32 v44, 16, v40
	v_pk_mul_f32 v[40:41], v[16:17], v[46:47] op_sel_hi:[0,1]
	v_and_b32_e32 v47, 0xffff0000, v42
	v_lshlrev_b32_e32 v46, 16, v42
	v_pk_mul_f32 v[42:43], v[16:17], v[52:53] op_sel_hi:[0,1]
	v_add3_u32 v54, v54, v58, s73
	v_add3_u32 v55, v55, v57, s73
	v_pk_mul_f32 v[44:45], v[16:17], v[44:45] op_sel_hi:[0,1]
	v_pk_mul_f32 v[46:47], v[16:17], v[46:47] op_sel_hi:[0,1]
	v_bfe_u32 v17, v43, 16, 1
	v_bfe_u32 v52, v42, 16, 1
	v_perm_b32 v86, v55, v54, s72
	v_bfe_u32 v55, v41, 16, 1
	v_bfe_u32 v56, v40, 16, 1
	v_bfe_u32 v57, v45, 16, 1
	v_bfe_u32 v58, v44, 16, 1
	v_add3_u32 v42, v42, v52, s73
	v_add3_u32 v17, v43, v17, s73
	v_add3_u32 v44, v44, v58, s73
	v_add3_u32 v45, v45, v57, s73
	v_add3_u32 v40, v40, v56, s73
	v_add3_u32 v41, v41, v55, s73
	v_perm_b32 v91, v17, v42, s72
	v_and_b32_e32 v43, 0xffff0000, v37
	v_lshlrev_b32_e32 v42, 16, v37
	v_perm_b32 v89, v41, v40, s72
	v_perm_b32 v88, v45, v44, s72
	v_and_b32_e32 v41, 0xffff0000, v36
	v_lshlrev_b32_e32 v40, 16, v36
	v_pk_mul_f32 v[36:37], v[16:17], v[42:43] op_sel_hi:[0,1]
	v_and_b32_e32 v43, 0xffff0000, v38
	v_lshlrev_b32_e32 v42, 16, v38
	v_and_b32_e32 v45, 0xffff0000, v39
	v_lshlrev_b32_e32 v44, 16, v39
	v_bfe_u32 v53, v47, 16, 1
	v_bfe_u32 v54, v46, 16, 1
	v_pk_mul_f32 v[40:41], v[16:17], v[40:41] op_sel_hi:[0,1]
	v_pk_mul_f32 v[42:43], v[16:17], v[42:43] op_sel_hi:[0,1]
	v_pk_mul_f32 v[16:17], v[16:17], v[44:45] op_sel_hi:[0,1]
	v_add3_u32 v46, v46, v54, s73
	v_add3_u32 v47, v47, v53, s73
	v_bfe_u32 v38, v17, 16, 1
	v_bfe_u32 v39, v16, 16, 1
	v_perm_b32 v90, v47, v46, s72
	v_bfe_u32 v46, v37, 16, 1
	v_bfe_u32 v47, v36, 16, 1
	v_bfe_u32 v52, v41, 16, 1
	v_bfe_u32 v53, v40, 16, 1
; __device__ __forceinline__ bf16 f2bf(float f) { unsigned u = __float_as_uint(f); return (bf16)((u + 0x7fffu + ((u >> 16) & 1u)) >> 16); }
; __device__ __forceinline__ bool run_unit2(LAS unsigned char* lds, const bf16* y0, const float* aux, unsigned* maskg, int b, int g, int tid_in, int wave, int lane) {
;     ...
;     for (int hd = 0; hd < 4; ++hd) {
;         const float wsc = w4[hd] * 0.0625f;
;         lo4[hd] = (w4[hd] >= 0.f) ? 0.f : -INFINITY; hi4[hd] = (w4[hd] >= 0.f) ? INFINITY : 0.f;
; #pragma unroll
;         for (int s = 0; s < 4; ++s) {
;             bf16x8 a = qf[hd][s];
; #pragma unroll
;             for (int j = 0; j < 8; ++j) a[j] = (short)f2bf(__uint_as_float(((unsigned)(unsigned short)a[j]) << 16) * wsc);
;             qf[hd][s] = a;
;         }
;     }
	v_add3_u32 v16, v16, v39, s73
	v_add3_u32 v17, v17, v38, s73
	v_bfe_u32 v44, v43, 16, 1
	v_bfe_u32 v45, v42, 16, 1
	v_add3_u32 v40, v40, v53, s73
	v_add3_u32 v41, v41, v52, s73
	v_add3_u32 v36, v36, v47, s73
	v_add3_u32 v37, v37, v46, s73
	v_perm_b32 v95, v17, v16, s72
	v_mul_f32_e32 v16, 0x3d800000, v18
	v_and_b32_e32 v39, 0xffff0000, v33
	v_lshlrev_b32_e32 v38, 16, v33
	v_add3_u32 v42, v42, v45, s73
	v_add3_u32 v43, v43, v44, s73
	v_perm_b32 v93, v37, v36, s72
	v_perm_b32 v92, v41, v40, s72
	v_and_b32_e32 v37, 0xffff0000, v32
	v_lshlrev_b32_e32 v36, 16, v32
	v_pk_mul_f32 v[32:33], v[16:17], v[38:39] op_sel_hi:[0,1]
	v_and_b32_e32 v41, 0xffff0000, v35
	v_lshlrev_b32_e32 v40, 16, v35
	v_perm_b32 v94, v43, v42, s72
	v_pk_mul_f32 v[36:37], v[16:17], v[36:37] op_sel_hi:[0,1]
	v_and_b32_e32 v39, 0xffff0000, v34
	v_lshlrev_b32_e32 v38, 16, v34
	v_pk_mul_f32 v[34:35], v[16:17], v[40:41] op_sel_hi:[0,1]
	v_bfe_u32 v42, v33, 16, 1
	v_bfe_u32 v43, v32, 16, 1
	v_cndmask_b32_e64 v209, v188, 0, vcc
	v_cndmask_b32_e32 v210, 0, v189, vcc
	v_cmp_le_f32_e32 vcc, 0, v18
	v_pk_mul_f32 v[38:39], v[16:17], v[38:39] op_sel_hi:[0,1]
	v_bfe_u32 v17, v35, 16, 1
	v_bfe_u32 v18, v34, 16, 1
	v_bfe_u32 v44, v37, 16, 1
	v_bfe_u32 v45, v36, 16, 1
	v_add3_u32 v32, v32, v43, s73
	v_add3_u32 v33, v33, v42, s73
	v_bfe_u32 v40, v39, 16, 1
	v_bfe_u32 v41, v38, 16, 1
	v_add3_u32 v36, v36, v45, s73
	v_add3_u32 v37, v37, v44, s73
	v_add3_u32 v18, v34, v18, s73
	v_add3_u32 v17, v35, v17, s73
	v_perm_b32 v97, v33, v32, s72
	v_and_b32_e32 v33, 0xffff0000, v28
	v_lshlrev_b32_e32 v32, 16, v28
	v_and_b32_e32 v35, 0xffff0000, v29
	v_lshlrev_b32_e32 v34, 16, v29
	v_add3_u32 v38, v38, v41, s73
	v_add3_u32 v39, v39, v40, s73
	v_perm_b32 v96, v37, v36, s72
	v_pk_mul_f32 v[32:33], v[16:17], v[32:33] op_sel_hi:[0,1]
	v_pk_mul_f32 v[28:29], v[16:17], v[34:35] op_sel_hi:[0,1]
	v_and_b32_e32 v37, 0xffff0000, v31
	v_lshlrev_b32_e32 v36, 16, v31
	v_perm_b32 v98, v39, v38, s72
	v_and_b32_e32 v35, 0xffff0000, v30
	v_lshlrev_b32_e32 v34, 16, v30
	v_pk_mul_f32 v[30:31], v[16:17], v[36:37] op_sel_hi:[0,1]
	v_bfe_u32 v38, v29, 16, 1
	v_bfe_u32 v39, v28, 16, 1
	v_bfe_u32 v40, v33, 16, 1
	v_bfe_u32 v41, v32, 16, 1
	v_perm_b32 v99, v17, v18, s72
	v_pk_mul_f32 v[34:35], v[16:17], v[34:35] op_sel_hi:[0,1]
	v_bfe_u32 v17, v31, 16, 1
	v_bfe_u32 v18, v30, 16, 1
	v_add3_u32 v32, v32, v41, s73
	v_add3_u32 v33, v33, v40, s73
	v_add3_u32 v28, v28, v39, s73
	v_add3_u32 v29, v29, v38, s73
	v_bfe_u32 v36, v35, 16, 1
	v_bfe_u32 v37, v34, 16, 1
	v_add3_u32 v18, v30, v18, s73
	v_add3_u32 v17, v31, v17, s73
	v_perm_b32 v101, v29, v28, s72
	v_perm_b32 v100, v33, v32, s72
	v_and_b32_e32 v29, 0xffff0000, v24
	v_lshlrev_b32_e32 v28, 16, v24
	v_and_b32_e32 v31, 0xffff0000, v25
	v_lshlrev_b32_e32 v30, 16, v25
	v_and_b32_e32 v33, 0xffff0000, v27
	v_lshlrev_b32_e32 v32, 16, v27
	v_add3_u32 v34, v34, v37, s73
	v_add3_u32 v35, v35, v36, s73
	v_pk_mul_f32 v[28:29], v[16:17], v[28:29] op_sel_hi:[0,1]
	v_pk_mul_f32 v[24:25], v[16:17], v[30:31] op_sel_hi:[0,1]
	v_and_b32_e32 v31, 0xffff0000, v26
	v_lshlrev_b32_e32 v30, 16, v26
	v_pk_mul_f32 v[26:27], v[16:17], v[32:33] op_sel_hi:[0,1]
	v_perm_b32 v103, v17, v18, s72
	v_perm_b32 v102, v35, v34, s72
	v_pk_mul_f32 v[30:31], v[16:17], v[30:31] op_sel_hi:[0,1]
	v_bfe_u32 v17, v27, 16, 1
	v_bfe_u32 v18, v26, 16, 1
	v_bfe_u32 v34, v25, 16, 1
	v_bfe_u32 v35, v24, 16, 1
	v_bfe_u32 v36, v29, 16, 1
	v_bfe_u32 v37, v28, 16, 1
	v_add3_u32 v28, v28, v37, s73
	v_add3_u32 v29, v29, v36, s73
	v_add3_u32 v24, v24, v35, s73
	v_add3_u32 v25, v25, v34, s73
	v_add3_u32 v18, v26, v18, s73
	v_add3_u32 v17, v27, v17, s73
	v_and_b32_e32 v27, 0xffff0000, v21
	v_lshlrev_b32_e32 v26, 16, v21
	v_bfe_u32 v32, v31, 16, 1
	v_bfe_u32 v33, v30, 16, 1
	v_perm_b32 v105, v25, v24, s72
	v_perm_b32 v104, v29, v28, s72
	v_and_b32_e32 v25, 0xffff0000, v20
	v_lshlrev_b32_e32 v24, 16, v20
	v_pk_mul_f32 v[20:21], v[16:17], v[26:27] op_sel_hi:[0,1]
	v_and_b32_e32 v27, 0xffff0000, v22
	v_lshlrev_b32_e32 v26, 16, v22
	v_and_b32_e32 v29, 0xffff0000, v23
	v_lshlrev_b32_e32 v28, 16, v23
	v_add3_u32 v30, v30, v33, s73
	v_add3_u32 v31, v31, v32, s73
	v_perm_b32 v107, v17, v18, s72
	v_pk_mul_f32 v[24:25], v[16:17], v[24:25] op_sel_hi:[0,1]
	v_pk_mul_f32 v[26:27], v[16:17], v[26:27] op_sel_hi:[0,1]
	v_pk_mul_f32 v[16:17], v[16:17], v[28:29] op_sel_hi:[0,1]
	v_perm_b32 v106, v31, v30, s72
	v_bfe_u32 v18, v17, 16, 1
	v_bfe_u32 v22, v16, 16, 1
	v_bfe_u32 v23, v27, 16, 1
	v_bfe_u32 v28, v26, 16, 1
	v_bfe_u32 v29, v21, 16, 1
	v_bfe_u32 v30, v20, 16, 1
	v_add3_u32 v20, v20, v30, s73
	v_add3_u32 v21, v21, v29, s73
	v_add3_u32 v26, v26, v28, s73
	v_add3_u32 v23, v27, v23, s73
	v_add3_u32 v16, v16, v22, s73
	v_add3_u32 v17, v17, v18, s73
	v_cndmask_b32_e64 v212, v188, 0, vcc
	v_cndmask_b32_e32 v213, 0, v189, vcc
	v_bfe_u32 v31, v25, 16, 1
	v_bfe_u32 v32, v24, 16, 1
	v_perm_b32 v111, v17, v16, s72
	v_perm_b32 v110, v23, v26, s72
	v_perm_b32 v109, v21, v20, s72
; __device__ __forceinline__ bf16 f2bf(float f) { unsigned u = __float_as_uint(f); return (bf16)((u + 0x7fffu + ((u >> 16) & 1u)) >> 16); }
; #define DSA2_LOADK(dst, kt_) do { _Pragma("unroll") for (int s = 0; s < 4; ++s) dst[s] = *(const bf16x8*)(kp + (size_t)(32 * (kt_)) * Y0P + 16 * s); } while (0)
; template <int STAGE>
; __device__ __forceinline__ void pass2(LAS unsigned char* lds, const bf16* kbase, int g, int t0, const bf16x8 (&qf)[4][4], const f32x4 lo4, const f32x4 hi4, int wave, int r, int h2) {
;     ...
;     int kt = wave;
;     if (kt <= g) DSA2_LOADK(kf, kt);
;     for (;;) {
;         if (kt > g) break;
;         if (kt + 8 <= g) DSA2_LOADK(kn, kt + 8);
; __device__ __forceinline__ bool run_unit2(LAS unsigned char* lds, const bf16* y0, const float* aux, unsigned* maskg, int b, int g, int tid_in, int wave, int lane) {
;     ...
;     for (int hd = 0; hd < 4; ++hd) {
;         const float wsc = w4[hd] * 0.0625f;
;         lo4[hd] = (w4[hd] >= 0.f) ? 0.f : -INFINITY; hi4[hd] = (w4[hd] >= 0.f) ? INFINITY : 0.f;
; #pragma unroll
;         for (int s = 0; s < 4; ++s) {
;             bf16x8 a = qf[hd][s];
; #pragma unroll
;             for (int j = 0; j < 8; ++j) a[j] = (short)f2bf(__uint_as_float(((unsigned)(unsigned short)a[j]) << 16) * wsc);
;             qf[hd][s] = a;
;         }
;     }
	v_mul_f32_e32 v16, 0x3d800000, v19
	v_cmp_le_f32_e32 vcc, 0, v19
	v_and_b32_e32 v19, 0xffff0000, v12
	v_lshlrev_b32_e32 v18, 16, v12
	v_and_b32_e32 v21, 0xffff0000, v13
	v_lshlrev_b32_e32 v20, 16, v13
	v_and_b32_e32 v23, 0xffff0000, v15
	v_lshlrev_b32_e32 v22, 16, v15
	v_add3_u32 v24, v24, v32, s73
	v_add3_u32 v25, v25, v31, s73
	v_pk_mul_f32 v[18:19], v[16:17], v[18:19] op_sel_hi:[0,1]
	v_pk_mul_f32 v[12:13], v[16:17], v[20:21] op_sel_hi:[0,1]
	v_and_b32_e32 v21, 0xffff0000, v14
	v_lshlrev_b32_e32 v20, 16, v14
	v_pk_mul_f32 v[14:15], v[16:17], v[22:23] op_sel_hi:[0,1]
	v_perm_b32 v108, v25, v24, s72
	v_pk_mul_f32 v[20:21], v[16:17], v[20:21] op_sel_hi:[0,1]
	v_bfe_u32 v17, v15, 16, 1
	v_bfe_u32 v22, v14, 16, 1
	v_bfe_u32 v25, v13, 16, 1
	v_bfe_u32 v26, v12, 16, 1
	v_bfe_u32 v27, v19, 16, 1
	v_bfe_u32 v28, v18, 16, 1
	v_add3_u32 v18, v18, v28, s73
	v_add3_u32 v19, v19, v27, s73
	v_add3_u32 v12, v12, v26, s73
	v_add3_u32 v13, v13, v25, s73
	v_add3_u32 v14, v14, v22, s73
	v_add3_u32 v15, v15, v17, s73
	v_perm_b32 v115, v15, v14, s72
	v_perm_b32 v113, v13, v12, s72
	v_perm_b32 v112, v19, v18, s72
	v_and_b32_e32 v13, 0xffff0000, v8
	v_lshlrev_b32_e32 v12, 16, v8
	v_and_b32_e32 v15, 0xffff0000, v9
	v_lshlrev_b32_e32 v14, 16, v9
	v_and_b32_e32 v19, 0xffff0000, v11
	v_lshlrev_b32_e32 v18, 16, v11
	v_bfe_u32 v23, v21, 16, 1
	v_bfe_u32 v24, v20, 16, 1
	v_pk_mul_f32 v[12:13], v[16:17], v[12:13] op_sel_hi:[0,1]
	v_pk_mul_f32 v[8:9], v[16:17], v[14:15] op_sel_hi:[0,1]
	v_and_b32_e32 v15, 0xffff0000, v10
	v_lshlrev_b32_e32 v14, 16, v10
	v_pk_mul_f32 v[10:11], v[16:17], v[18:19] op_sel_hi:[0,1]
	v_add3_u32 v20, v20, v24, s73
	v_add3_u32 v21, v21, v23, s73
	v_pk_mul_f32 v[14:15], v[16:17], v[14:15] op_sel_hi:[0,1]
	v_bfe_u32 v17, v11, 16, 1
	v_bfe_u32 v18, v10, 16, 1
	v_bfe_u32 v23, v13, 16, 1
	v_bfe_u32 v24, v12, 16, 1
	v_perm_b32 v114, v21, v20, s72
	v_bfe_u32 v21, v9, 16, 1
	v_bfe_u32 v22, v8, 16, 1
	v_add3_u32 v12, v12, v24, s73
	v_add3_u32 v13, v13, v23, s73
	v_add3_u32 v10, v10, v18, s73
	v_add3_u32 v11, v11, v17, s73
	v_add3_u32 v8, v8, v22, s73
	v_add3_u32 v9, v9, v21, s73
	v_perm_b32 v119, v11, v10, s72
	v_perm_b32 v116, v13, v12, s72
	v_and_b32_e32 v11, 0xffff0000, v5
	v_lshlrev_b32_e32 v10, 16, v5
	v_and_b32_e32 v13, 0xffff0000, v7
	v_lshlrev_b32_e32 v12, 16, v7
	v_perm_b32 v117, v9, v8, s72
	v_and_b32_e32 v9, 0xffff0000, v4
	v_lshlrev_b32_e32 v8, 16, v4
	v_pk_mul_f32 v[4:5], v[16:17], v[10:11] op_sel_hi:[0,1]
	v_and_b32_e32 v11, 0xffff0000, v6
	v_lshlrev_b32_e32 v10, 16, v6
	v_pk_mul_f32 v[6:7], v[16:17], v[12:13] op_sel_hi:[0,1]
	v_bfe_u32 v19, v15, 16, 1
	v_bfe_u32 v20, v14, 16, 1
	v_pk_mul_f32 v[8:9], v[16:17], v[8:9] op_sel_hi:[0,1]
	v_bfe_u32 v12, v7, 16, 1
	v_bfe_u32 v13, v6, 16, 1
	v_add3_u32 v14, v14, v20, s73
	v_add3_u32 v15, v15, v19, s73
	v_pk_mul_f32 v[10:11], v[16:17], v[10:11] op_sel_hi:[0,1]
	v_bfe_u32 v17, v5, 16, 1
	v_bfe_u32 v18, v4, 16, 1
	v_bfe_u32 v19, v9, 16, 1
	v_bfe_u32 v20, v8, 16, 1
	v_add3_u32 v6, v6, v13, s73
	v_add3_u32 v7, v7, v12, s73
	v_add3_u32 v8, v8, v20, s73
	v_add3_u32 v9, v9, v19, s73
	v_add3_u32 v4, v4, v18, s73
	v_add3_u32 v5, v5, v17, s73
	v_perm_b32 v123, v7, v6, s72
	v_and_b32_e32 v7, 0xffff0000, v1
	v_lshlrev_b32_e32 v6, 16, v1
	v_perm_b32 v118, v15, v14, s72
	v_bfe_u32 v14, v11, 16, 1
	v_bfe_u32 v15, v10, 16, 1
	v_perm_b32 v121, v5, v4, s72
	v_perm_b32 v120, v9, v8, s72
	v_and_b32_e32 v5, 0xffff0000, v0
	v_lshlrev_b32_e32 v4, 16, v0
	v_pk_mul_f32 v[0:1], v[16:17], v[6:7] op_sel_hi:[0,1]
	v_and_b32_e32 v7, 0xffff0000, v2
	v_lshlrev_b32_e32 v6, 16, v2
	v_and_b32_e32 v9, 0xffff0000, v3
	v_lshlrev_b32_e32 v8, 16, v3
	v_add3_u32 v10, v10, v15, s73
	v_add3_u32 v11, v11, v14, s73
	v_pk_mul_f32 v[4:5], v[16:17], v[4:5] op_sel_hi:[0,1]
	v_pk_mul_f32 v[6:7], v[16:17], v[6:7] op_sel_hi:[0,1]
	v_pk_mul_f32 v[2:3], v[16:17], v[8:9] op_sel_hi:[0,1]
	v_bfe_u32 v12, v1, 16, 1
	v_bfe_u32 v13, v0, 16, 1
	v_perm_b32 v122, v11, v10, s72
	v_bfe_u32 v8, v3, 16, 1
	v_bfe_u32 v9, v2, 16, 1
	v_bfe_u32 v10, v7, 16, 1
	v_bfe_u32 v11, v6, 16, 1
	v_bfe_u32 v14, v5, 16, 1
	v_bfe_u32 v15, v4, 16, 1
	v_add3_u32 v0, v0, v13, s73
	v_add3_u32 v1, v1, v12, s73
	v_add3_u32 v4, v4, v15, s73
	v_add3_u32 v5, v5, v14, s73
	v_add3_u32 v6, v6, v11, s73
	v_add3_u32 v7, v7, v10, s73
	v_add3_u32 v2, v2, v9, s73
	v_add3_u32 v3, v3, v8, s73
	v_perm_b32 v125, v1, v0, s72
	v_lshl_add_u64 v[0:1], s[80:81], 0, v[176:177]
	v_cndmask_b32_e64 v214, v188, 0, vcc
	v_cndmask_b32_e32 v215, 0, v189, vcc
	v_perm_b32 v127, v3, v2, s72
	v_perm_b32 v126, v7, v6, s72
	v_perm_b32 v124, v5, v4, s72
	v_lshl_add_u64 v[178:179], v[0:1], 0, v[50:51]
	s_cbranch_scc1 .LBB0_804
	v_lshl_add_u64 v[0:1], v[48:49], 1, s[78:79]
	v_lshl_add_u64 v[0:1], v[0:1], 0, v[176:177]
	v_mad_u32_u24 v204, v218, s26, 0
	v_lshl_add_u64 v[180:181], s[34:35], 0, v[0:1]
	s_sub_i32 s0, 0, s64
	s_mov_b32 s1, s30
	s_mov_b32 s6, s92
	v_readlane_b32 s98, v254, 24
	s_cmp_lt_u32 s98, 4
	s_cbranch_scc1 .Lp4stag0
	s_sleep 14
	s_setprio 1

; #define LAS __attribute__((address_space(3)))
; __device__ __forceinline__ bool run_unit2(LAS unsigned char* lds, const bf16* y0, const float* aux, unsigned* maskg, int b, int g, int tid_in, int wave, int lane) {
;     ...
;     {
;         const int q = tid >> 4, i = tid & 15;
;         unsigned c[30]; unsigned cs = 0u;
; #pragma unroll
;         for (int k = 0; k < 30; ++k) { c[k] = hist[q * HROW2 + 30 * i + k]; cs += c[k]; }
;         unsigned v = cs;
; #pragma unroll
;         for (int o = 1; o < 16; o <<= 1) { const unsigned t = (unsigned)__shfl_down((int)v, o, 16); if (i + o < 16) v += t; }
;         const unsigned above = v - cs;
;         if (i == 0) { const bool selall = (t0 + q) < 256; if (selall || v < 256u) { ((LAS int*)(lds + OFF2_TB))[q] = -1; ((LAS int*)(lds + OFF2_NEED))[q] = 0; } }
;         if (!((t0 + q) < 256) && above < 256u && 256u <= above + cs) {
;             unsigned cum = above; bool done = false;
; #pragma unroll
;             for (int k = 29; k >= 0; --k) { if (!done) { if (cum + c[k] >= 256u) { ((LAS int*)(lds + OFF2_TB))[q] = 30 * i + k; ((LAS int*)(lds + OFF2_NEED))[q] = (int)(256u - cum);
;                         if (c[k] > (unsigned)CAP2) ((LAS int*)(lds + OFF2_FLAG))[0] = 1; done = true; } else cum += c[k]; } }
;         }
.LBB0_804:
	s_setprio 0
	s_waitcnt vmcnt(0)
	v_ashrrev_i32_e32 v220, 4, v206
	v_and_b32_e32 v216, 15, v206
	v_mul_lo_u32 v0, v220, s26
	v_mul_u32_u24_e32 v1, 0x78, v216
	v_add3_u32 v28, 0, v0, v1
	s_waitcnt lgkmcnt(0)
	s_barrier
	ds_read2_b32 v[0:1], v28 offset1:1
	ds_read2_b32 v[2:3], v28 offset0:2 offset1:3
	ds_read2_b32 v[4:5], v28 offset0:4 offset1:5
	ds_read2_b32 v[6:7], v28 offset0:6 offset1:7
	v_and_b32_e32 v31, 15, v192
	s_waitcnt lgkmcnt(3)
	v_add_u32_e32 v8, v1, v0
	s_waitcnt lgkmcnt(2)
	v_add3_u32 v8, v8, v2, v3
	s_waitcnt lgkmcnt(1)
	v_add3_u32 v14, v8, v4, v5
	ds_read2_b32 v[8:9], v28 offset0:8 offset1:9
	ds_read2_b32 v[10:11], v28 offset0:10 offset1:11
	ds_read2_b32 v[12:13], v28 offset0:12 offset1:13
	s_waitcnt lgkmcnt(3)
	v_add3_u32 v16, v14, v6, v7
	ds_read2_b32 v[14:15], v28 offset0:14 offset1:15
	s_waitcnt lgkmcnt(3)
	v_add3_u32 v16, v16, v8, v9
	s_waitcnt lgkmcnt(2)
	v_add3_u32 v16, v16, v10, v11
	s_waitcnt lgkmcnt(1)
	v_add3_u32 v20, v16, v12, v13
	ds_read2_b32 v[16:17], v28 offset0:16 offset1:17
	ds_read2_b32 v[18:19], v28 offset0:18 offset1:19
	s_waitcnt lgkmcnt(2)
	v_add3_u32 v24, v20, v14, v15
	ds_read2_b32 v[20:21], v28 offset0:20 offset1:21
	ds_read2_b32 v[22:23], v28 offset0:22 offset1:23
	v_cmp_ne_u32_e32 vcc, 15, v31
	s_waitcnt lgkmcnt(3)
	v_add3_u32 v24, v24, v16, v17
	s_waitcnt lgkmcnt(2)
	v_add3_u32 v30, v24, v18, v19
	ds_read2_b32 v[24:25], v28 offset0:24 offset1:25
	ds_read2_b32 v[26:27], v28 offset0:26 offset1:27
	ds_read2_b32 v[28:29], v28 offset0:28 offset1:29
	s_waitcnt lgkmcnt(4)
	v_add3_u32 v30, v30, v20, v21
	s_waitcnt lgkmcnt(3)
	v_add3_u32 v30, v30, v22, v23
	s_waitcnt lgkmcnt(2)
	v_add3_u32 v30, v30, v24, v25
	s_waitcnt lgkmcnt(1)
	v_add3_u32 v30, v30, v26, v27
	v_addc_co_u32_e32 v31, vcc, 0, v192, vcc
	s_waitcnt lgkmcnt(0)
	v_add3_u32 v30, v30, v28, v29
	v_lshlrev_b32_e32 v180, 2, v31
	ds_bpermute_b32 v31, v180, v30
	v_bitop3_b32 v32, v192, 15, v192 bitop3:0xc
	v_cmp_ne_u32_e32 vcc, 15, v216
	v_lshl_add_u32 v221, v220, 2, 0
	s_waitcnt lgkmcnt(0)
	v_cndmask_b32_e32 v31, 0, v31, vcc
	v_cmp_gt_u32_e32 vcc, 2, v32
	v_add_u32_e32 v31, v31, v30
	s_nop 0
	v_cndmask_b32_e64 v33, 2, 0, vcc
	v_add_lshl_u32 v181, v33, v192, 2
	ds_bpermute_b32 v33, v181, v31
	v_cmp_gt_u32_e32 vcc, 14, v216
	s_waitcnt lgkmcnt(0)
	s_nop 0
	v_cndmask_b32_e32 v33, 0, v33, vcc
	v_cmp_gt_u32_e32 vcc, 4, v32
	v_add_u32_e32 v31, v33, v31
	s_nop 0
	v_cndmask_b32_e64 v32, 4, 0, vcc
	v_add_lshl_u32 v204, v32, v192, 2
	ds_bpermute_b32 v32, v204, v31
	v_cmp_gt_u32_e32 vcc, 12, v216
	s_waitcnt lgkmcnt(0)
	s_nop 0
	v_cndmask_b32_e32 v32, 0, v32, vcc
	v_add_u32_e32 v31, v32, v31
	v_bitop3_b32 v32, v192, 8, 15 bitop3:8
	v_add_lshl_u32 v205, v32, v192, 2
	ds_bpermute_b32 v32, v205, v31
	v_cmp_gt_u32_e32 vcc, 8, v216
	s_waitcnt lgkmcnt(0)
	s_nop 0
	v_cndmask_b32_e32 v32, 0, v32, vcc
	v_add_u32_e32 v31, v32, v31
	v_add_u32_e32 v32, s41, v220
	v_cmp_gt_i32_e64 s[2:3], s68, v32
	v_cmp_gt_u32_e64 s[4:5], s68, v31
	v_cmp_eq_u32_e32 vcc, 0, v216
	s_or_b64 s[0:1], s[2:3], s[4:5]
	s_and_b64 s[0:1], vcc, s[0:1]
	s_and_saveexec_b64 s[2:3], s[0:1]
	s_cbranch_execz .LBB0_806
	v_add_u32_e32 v34, 0x18100, v221
	v_add_u32_e32 v33, 0x18180, v221
	ds_write_b32 v34, v185
	ds_write_b32 v33, v177

; #define LAS __attribute__((address_space(3)))
; __device__ __forceinline__ int bin2(float sv, int zi) {
;     const unsigned u = __float_as_uint(sv);
;     int c = (int)((u >> 20) & 0x7FFu) - 832;
;     c = c < 0 ? 0 : (c > 207 ? 207 : c);
;     int b = (u >> 31) ? (207 - c) : (272 + c);
;     if (sv == 0.0f) b = 208 + zi;
;     return b;
; }
; template <int STAGE>
; __device__ __forceinline__ void pass2(LAS unsigned char* lds, const bf16* kbase, int g, int t0, const bf16x8 (&qf)[4][4], const f32x4 lo4, const f32x4 hi4, int wave, int r, int h2) {
;     LAS unsigned* hist = (LAS unsigned*)(lds + OFF2_HIST);
;     LAS unsigned long long* cand = (LAS unsigned long long*)(lds + OFF2_CAND);
;     LAS unsigned* gtm = (LAS unsigned*)(lds + OFF2_GT);
;     LAS unsigned* cntp = (LAS unsigned*)(lds + OFF2_CNT);
;     const int tq = t0 + r;
;     const int tb = (STAGE == 1) ? ((const LAS int*)(lds + OFF2_TB))[r] : 0;
;     bf16x8 kf[4], kn[4];
;     const bf16* kp = kbase + (size_t)r * Y0P + 8 * h2;
.LBB0_822:
	s_or_b64 exec, exec, s[4:5]
	s_andn2_b64 vcc, exec, s[82:83]
	s_waitcnt lgkmcnt(0)
	s_barrier
	s_cbranch_vccnz .LBB0_880
	v_lshlrev_b32_e32 v0, 2, v218
	v_add_u32_e32 v1, 0, v0
	v_add_u32_e32 v1, 0x18100, v1
	ds_read_b32 v222, v1
	s_add_i32 s0, 0, 0x18200
	v_lshlrev_b32_e32 v1, 9, v219
	v_lshlrev_b32_e32 v2, 4, v218
	v_add_u32_e32 v224, s0, v0
	v_mov_b32_e32 v0, s27
	v_add3_u32 v223, s65, v1, v2
	v_lshlrev_b32_e32 v219, 2, v219
	v_lshl_add_u32 v225, v218, 11, 0
	v_cmp_gt_u32_e64 s[84:85], 32, v217
	v_mad_u32_u24 v217, v218, s24, v0
	v_readlane_b32 s0, v254, 24
	s_waitcnt lgkmcnt(0)
	v_sub_u32_e32 v0, 0xcf, v222
	v_add_u32_e32 v0, 0x340, v0
	v_lshlrev_b32_e32 v0, 20, v0
	v_add_u32_e32 v0, 0x7fffffff, v0
	v_add_u32_e32 v1, 0x100000, v0
	v_add_u32_e32 v2, 0x230, v222
	v_lshlrev_b32_e32 v2, 20, v2
	v_add_u32_e32 v3, 0x100000, v2
	v_mov_b32_e32 v4, 0xff800000
	v_bfrev_b32_e32 v5, 1
	v_mov_b32_e32 v6, 1
	v_mov_b32_e32 v7, 0x7fc00000
	v_mov_b32_e32 v8, 0x7fffffff
	v_cmp_gt_i32_e32 vcc, 0, v222
	s_nop 1
	v_cndmask_b32_e32 v252, v0, v4, vcc
	v_cmp_eq_u32_e32 vcc, 0xcf, v222
	s_nop 1
	v_cndmask_b32_e32 v252, v252, v5, vcc
	v_cmp_lt_i32_e32 vcc, 0xcf, v222
	s_nop 1
	v_cndmask_b32_e32 v252, v252, v6, vcc
	v_cmp_lt_i32_e32 vcc, 0x10f, v222
	s_nop 1
	v_cndmask_b32_e32 v252, v252, v3, vcc
	v_cmp_eq_u32_e32 vcc, 0x1df, v222
	s_nop 1
	v_cndmask_b32_e32 v252, v252, v7, vcc
	v_cmp_gt_i32_e32 vcc, 1, v222
	s_nop 1
	v_cndmask_b32_e32 v253, v1, v4, vcc
	v_cmp_lt_i32_e32 vcc, 0xcf, v222
	s_nop 1
	v_cndmask_b32_e32 v253, v253, v6, vcc
	v_cmp_lt_i32_e32 vcc, 0x110, v222
	s_nop 1
	v_cndmask_b32_e32 v253, v253, v2, vcc
	v_cmp_lt_i32_e32 vcc, 0xcf, v222
	s_nop 1
	v_cndmask_b32_e32 v232, v8, v222, vcc
	v_cmp_lt_i32_e32 vcc, 0x10f, v222
	s_nop 1
	v_cndmask_b32_e32 v232, v232, v8, vcc
	s_cmp_lt_u32 s0, 4
	s_cbranch_scc1 .Lp4stag1
	s_sleep 14
	s_setprio 1

; #define LAS __attribute__((address_space(3)))
; __device__ __forceinline__ bool run_unit2(LAS unsigned char* lds, const bf16* y0, const float* aux, unsigned* maskg, int b, int g, int tid_in, int wave, int lane) {
;     ...
;     __syncthreads();
;     if (((const LAS int*)(lds + OFF2_FLAG))[0] != 0) { __syncthreads(); return false; }
;     for (int i = tid; i < 65536 / 4; i += NTHR) ((LAS unsigned*)lds)[i] = 0u;
;     __syncthreads();
;     pass2<1>(lds, kbase, g, t0, qf, lo4, hi4, wave, r, h2);
;     __syncthreads();
;     {
;         const int q = tid >> 4, i = tid & 15;
;         const LAS unsigned long long* cq = (const LAS unsigned long long*)(lds + OFF2_CAND) + q * CAP2;
;         const int n = (int)((const LAS unsigned*)(lds + OFF2_CNT))[q], need = ((const LAS int*)(lds + OFF2_NEED))[q];
;         for (int a_ = i; a_ < n; a_ += 16) {
.LBB0_880:
	s_setprio 0
	s_waitcnt vmcnt(0)
	v_add_u32_e32 v0, 0x18200, v221
	s_waitcnt lgkmcnt(0)
	s_barrier
	ds_read_b32 v2, v0
	s_waitcnt lgkmcnt(0)
	v_cmp_lt_i32_e32 vcc, v216, v2
	s_and_saveexec_b64 s[4:5], vcc
	s_cbranch_execz .LBB0_887
	v_add_u32_e32 v0, 0x18180, v221
	ds_read_b32 v4, v0
	v_add_u32_e32 v0, 7, v2
	v_and_b32_e32 v5, -8, v0
	v_mul_lo_u32 v0, v220, s24
	v_lshl_add_u32 v3, v220, 11, 0
	v_add_u32_e32 v6, s27, v0
	s_mov_b64 s[6:7], 0
	s_branch .LBB0_883
